# v27 + down-GEMM epilogue: the eight row-info LDS reads of a unit issued together
# speedup vs baseline: 1.0017x; 1.0017x over previous
; #define LAS __attribute__((address_space(3)))
;     __device__ __forceinline__ void operator()(const f32x4 (&acc)[2][2][4][2], const pg8::Unit& u, int wr, int wc, int fr, int fq) const {
;         asm volatile("" : "+v"(fr), "+v"(fq));
;         const unsigned c0b = (unsigned)((u.pn & 3) * 256 + wc * 64 + 16 * fq); const bool shared = (u.pn >> 2) == 256;
;         const LAS u32x2* ri = (const LAS u32x2*)(lds + MOE_RI_OFF) + u.ord * 256 + wr * 64 + fr;
; #pragma unroll
;         for (int ai = 0; ai < 2; ++ai)
; #pragma unroll
;             for (int m = 0; m < 4; ++m) { const u32x2 en = ri[ai * 128 + m * 16]; const float wv = __uint_as_float(en.y) * (YB_SCALE / (H8_SCALE * W8_SCALE));
;                 if ((int)en.x >= 0) { unsigned char* rp = YB + (size_t)(en.x * 1024u + c0b);
;                     const f32x4 v00 = acc[ai][0][m][0] * wv, v01 = acc[ai][0][m][1] * wv, v10 = acc[ai][1][m][0] * wv, v11 = acc[ai][1][m][1] * wv;
;                     const u32x2 h0 = pack8_fp8(v00, v01), h1 = pack8_fp8(v10, v11);
;                     *(u32x4*)rp = (u32x4){h0.x, h0.y, h1.x, h1.y};
.LBB0_888:
	s_lshl_b32 s15, s55, 11
	v_mov_b32_e32 v130, v137
	v_mov_b32_e32 v144, v138
	s_add_i32 s15, s46, s15
	s_lshl_b32 s14, s14, 8
	v_lshl_add_u32 v145, v130, 3, s15
	ds_read_b64 v[130:131], v145
	ds_read_b64 v[152:153], v145 offset:128
	ds_read_b64 v[154:155], v145 offset:256
	ds_read_b64 v[156:157], v145 offset:384
	ds_read_b64 v[158:159], v145 offset:1024
	ds_read_b64 v[160:161], v145 offset:1152
	ds_read_b64 v[162:163], v145 offset:1280
	ds_read_b64 v[164:165], v145 offset:1408
	s_and_b32 s14, s14, 0x300
	s_or_b32 s14, s14, s45
	v_lshl_add_u32 v144, v144, 4, s14
	s_waitcnt lgkmcnt(0)
	v_cmp_lt_i32_e32 vcc, -1, v130
	s_and_saveexec_b64 s[14:15], vcc
	s_cbranch_execz .LBB0_890
	v_mul_f32_e32 v146, 0x3c800000, v131
	v_pk_mul_f32 v[148:149], v[116:117], v[146:147] op_sel_hi:[1,0]
	v_pk_mul_f32 v[116:117], v[114:115], v[146:147] op_sel_hi:[1,0]
	v_mov_b32_e32 v114, 0
	v_pk_mul_f32 v[118:119], v[118:119], v[146:147] op_sel_hi:[1,0]
	v_pk_mul_f32 v[122:123], v[122:123], v[146:147] op_sel_hi:[1,0]
	v_pk_mul_f32 v[126:127], v[126:127], v[146:147] op_sel_hi:[1,0]
	v_cvt_pk_fp8_f32 v114, v116, v117
	v_mov_b32_e32 v115, 0
	v_mov_b32_e32 v116, 0
	v_mov_b32_e32 v117, 0
	v_cvt_pk_fp8_f32 v115, v118, v119
	v_cvt_pk_fp8_f32 v116, v122, v123
	v_cvt_pk_fp8_f32 v117, v126, v127
	v_pk_mul_f32 v[120:121], v[120:121], v[146:147] op_sel_hi:[1,0]
	v_pk_mul_f32 v[124:125], v[124:125], v[146:147] op_sel_hi:[1,0]
	v_pk_mul_f32 v[128:129], v[128:129], v[146:147] op_sel_hi:[1,0]
	v_cvt_pk_fp8_f32 v114, v148, v149 op_sel:[0,0,1]
	v_cvt_pk_fp8_f32 v115, v120, v121 op_sel:[0,0,1]
	v_cvt_pk_fp8_f32 v116, v124, v125 op_sel:[0,0,1]
	v_cvt_pk_fp8_f32 v117, v128, v129 op_sel:[0,0,1]
	v_lshl_add_u32 v118, v130, 10, v144
	global_store_dwordx4 v118, v[114:117], s[4:5]
.LBB0_890:
	s_or_b64 exec, exec, s[14:15]
	s_nop 1
	v_mov_b32_e32 v114, v152
	v_mov_b32_e32 v115, v153
	s_waitcnt lgkmcnt(0)
	v_cmp_lt_i32_e32 vcc, -1, v114
	s_and_saveexec_b64 s[14:15], vcc
	s_load_dwordx2 s[58:59], s[82:83], 0x118
	s_cbranch_execz .LBB0_892
	v_mul_f32_e32 v116, 0x3c800000, v115
	v_pk_mul_f32 v[118:119], v[100:101], v[116:117] op_sel_hi:[1,0]
	v_pk_mul_f32 v[100:101], v[98:99], v[116:117] op_sel_hi:[1,0]
	v_mov_b32_e32 v99, 0
	v_pk_mul_f32 v[102:103], v[102:103], v[116:117] op_sel_hi:[1,0]
	v_pk_mul_f32 v[110:111], v[110:111], v[116:117] op_sel_hi:[1,0]
	v_pk_mul_f32 v[106:107], v[106:107], v[116:117] op_sel_hi:[1,0]
	v_mov_b32_e32 v98, 0
	v_cvt_pk_fp8_f32 v99, v100, v101
	v_mov_b32_e32 v100, 0
	v_mov_b32_e32 v101, 0
	v_cvt_pk_fp8_f32 v98, v102, v103
	v_cvt_pk_fp8_f32 v100, v110, v111
	v_cvt_pk_fp8_f32 v101, v106, v107
	v_pk_mul_f32 v[104:105], v[104:105], v[116:117] op_sel_hi:[1,0]
	v_pk_mul_f32 v[112:113], v[112:113], v[116:117] op_sel_hi:[1,0]
	v_pk_mul_f32 v[108:109], v[108:109], v[116:117] op_sel_hi:[1,0]
	v_cvt_pk_fp8_f32 v98, v104, v105 op_sel:[0,0,1]
	v_cvt_pk_fp8_f32 v99, v118, v119 op_sel:[0,0,1]
	v_cvt_pk_fp8_f32 v100, v112, v113 op_sel:[0,0,1]
	v_cvt_pk_fp8_f32 v101, v108, v109 op_sel:[0,0,1]
	v_lshl_add_u32 v102, v114, 10, v144
	global_store_dwordx4 v102, v[98:101], s[4:5]
.LBB0_892:
	s_or_b64 exec, exec, s[14:15]
	s_nop 1
	v_mov_b32_e32 v98, v154
	v_mov_b32_e32 v99, v155
	s_waitcnt lgkmcnt(0)
	v_cmp_lt_i32_e32 vcc, -1, v98
	s_and_saveexec_b64 s[14:15], vcc
	s_cbranch_execz .LBB0_894
	v_mul_f32_e32 v100, 0x3c800000, v99
	v_pk_mul_f32 v[102:103], v[76:77], v[100:101] op_sel_hi:[1,0]
	v_pk_mul_f32 v[76:77], v[74:75], v[100:101] op_sel_hi:[1,0]
	v_mov_b32_e32 v75, 0
	v_pk_mul_f32 v[78:79], v[78:79], v[100:101] op_sel_hi:[1,0]
	v_pk_mul_f32 v[94:95], v[94:95], v[100:101] op_sel_hi:[1,0]
	v_pk_mul_f32 v[90:91], v[90:91], v[100:101] op_sel_hi:[1,0]
	v_mov_b32_e32 v74, 0
	v_cvt_pk_fp8_f32 v75, v76, v77
	v_mov_b32_e32 v76, 0
	v_mov_b32_e32 v77, 0
	v_cvt_pk_fp8_f32 v74, v78, v79
	v_cvt_pk_fp8_f32 v76, v94, v95
	v_cvt_pk_fp8_f32 v77, v90, v91
	v_pk_mul_f32 v[80:81], v[80:81], v[100:101] op_sel_hi:[1,0]
	v_pk_mul_f32 v[96:97], v[96:97], v[100:101] op_sel_hi:[1,0]
	v_pk_mul_f32 v[92:93], v[92:93], v[100:101] op_sel_hi:[1,0]
	v_cvt_pk_fp8_f32 v74, v80, v81 op_sel:[0,0,1]
	v_cvt_pk_fp8_f32 v75, v102, v103 op_sel:[0,0,1]
	v_cvt_pk_fp8_f32 v76, v96, v97 op_sel:[0,0,1]
	v_cvt_pk_fp8_f32 v77, v92, v93 op_sel:[0,0,1]
	v_lshl_add_u32 v78, v98, 10, v144
	global_store_dwordx4 v78, v[74:77], s[4:5]
.LBB0_894:
	s_or_b64 exec, exec, s[14:15]
	s_nop 1
	v_mov_b32_e32 v74, v156
	v_mov_b32_e32 v75, v157
	s_waitcnt lgkmcnt(0)
	v_cmp_lt_i32_e32 vcc, -1, v74
	s_and_saveexec_b64 s[14:15], vcc
	s_cbranch_execz .LBB0_896
	v_mul_f32_e32 v76, 0x3c800000, v75
	v_pk_mul_f32 v[78:79], v[44:45], v[76:77] op_sel_hi:[1,0]
	v_pk_mul_f32 v[44:45], v[42:43], v[76:77] op_sel_hi:[1,0]
	v_mov_b32_e32 v43, 0
	v_pk_mul_f32 v[46:47], v[46:47], v[76:77] op_sel_hi:[1,0]
	v_pk_mul_f32 v[62:63], v[62:63], v[76:77] op_sel_hi:[1,0]
	v_pk_mul_f32 v[58:59], v[58:59], v[76:77] op_sel_hi:[1,0]
	v_mov_b32_e32 v42, 0
	v_cvt_pk_fp8_f32 v43, v44, v45
	v_mov_b32_e32 v44, 0
	v_mov_b32_e32 v45, 0
	v_cvt_pk_fp8_f32 v42, v46, v47
	v_cvt_pk_fp8_f32 v44, v62, v63
	v_cvt_pk_fp8_f32 v45, v58, v59
	v_pk_mul_f32 v[48:49], v[48:49], v[76:77] op_sel_hi:[1,0]
	v_pk_mul_f32 v[64:65], v[64:65], v[76:77] op_sel_hi:[1,0]
	v_pk_mul_f32 v[60:61], v[60:61], v[76:77] op_sel_hi:[1,0]
	v_cvt_pk_fp8_f32 v42, v48, v49 op_sel:[0,0,1]
	v_cvt_pk_fp8_f32 v43, v78, v79 op_sel:[0,0,1]
	v_cvt_pk_fp8_f32 v44, v64, v65 op_sel:[0,0,1]
	v_cvt_pk_fp8_f32 v45, v60, v61 op_sel:[0,0,1]
	v_lshl_add_u32 v46, v74, 10, v144
	global_store_dwordx4 v46, v[42:45], s[4:5]
;     __device__ __forceinline__ void operator()(const f32x4 (&acc)[2][2][4][2], const pg8::Unit& u, int wr, int wc, int fr, int fq) const {
;     ...
;         for (int ai = 0; ai < 2; ++ai)
; #pragma unroll
;             for (int m = 0; m < 4; ++m) { const u32x2 en = ri[ai * 128 + m * 16]; const float wv = __uint_as_float(en.y) * (YB_SCALE / (H8_SCALE * W8_SCALE));
;                 if ((int)en.x >= 0) { unsigned char* rp = YB + (size_t)(en.x * 1024u + c0b);
;                     const f32x4 v00 = acc[ai][0][m][0] * wv, v01 = acc[ai][0][m][1] * wv, v10 = acc[ai][1][m][0] * wv, v11 = acc[ai][1][m][1] * wv;
;                     const u32x2 h0 = pack8_fp8(v00, v01), h1 = pack8_fp8(v10, v11);
;                     *(u32x4*)rp = (u32x4){h0.x, h0.y, h1.x, h1.y};
.LBB0_896:
	s_or_b64 exec, exec, s[14:15]
	s_nop 1
	v_mov_b32_e32 v42, v158
	v_mov_b32_e32 v43, v159
	s_waitcnt lgkmcnt(0)
	v_cmp_lt_i32_e32 vcc, -1, v42
	s_and_saveexec_b64 s[14:15], vcc
	s_cbranch_execz .LBB0_898
	v_mul_f32_e32 v44, 0x3c800000, v43
	v_pk_mul_f32 v[48:49], v[72:73], v[44:45] op_sel_hi:[1,0]
	v_pk_mul_f32 v[46:47], v[70:71], v[44:45] op_sel_hi:[1,0]
	v_pk_mul_f32 v[58:59], v[68:69], v[44:45] op_sel_hi:[1,0]
	v_pk_mul_f32 v[60:61], v[66:67], v[44:45] op_sel_hi:[1,0]
	v_pk_mul_f32 v[62:63], v[88:89], v[44:45] op_sel_hi:[1,0]
	v_pk_mul_f32 v[64:65], v[86:87], v[44:45] op_sel_hi:[1,0]
	v_pk_mul_f32 v[66:67], v[84:85], v[44:45] op_sel_hi:[1,0]
	v_pk_mul_f32 v[68:69], v[82:83], v[44:45] op_sel_hi:[1,0]
	v_mov_b32_e32 v44, 0
	v_cvt_pk_fp8_f32 v44, v46, v47
	v_mov_b32_e32 v45, 0
	v_mov_b32_e32 v46, 0
	v_mov_b32_e32 v47, 0
	v_cvt_pk_fp8_f32 v45, v60, v61
	v_cvt_pk_fp8_f32 v46, v64, v65
	v_cvt_pk_fp8_f32 v47, v68, v69
	v_cvt_pk_fp8_f32 v44, v48, v49 op_sel:[0,0,1]
	v_cvt_pk_fp8_f32 v45, v58, v59 op_sel:[0,0,1]
	v_cvt_pk_fp8_f32 v46, v62, v63 op_sel:[0,0,1]
	v_cvt_pk_fp8_f32 v47, v66, v67 op_sel:[0,0,1]
	v_lshl_add_u32 v42, v42, 10, v144
	global_store_dwordx4 v42, v[44:47], s[4:5]
.LBB0_898:
	s_or_b64 exec, exec, s[14:15]
	s_nop 1
	v_mov_b32_e32 v42, v160
	v_mov_b32_e32 v43, v161
	s_waitcnt lgkmcnt(0)
	v_cmp_lt_i32_e32 vcc, -1, v42
	s_and_saveexec_b64 s[14:15], vcc
	s_cbranch_execz .LBB0_900
	v_mul_f32_e32 v44, 0x3c800000, v43
	v_pk_mul_f32 v[46:47], v[36:37], v[44:45] op_sel_hi:[1,0]
	v_pk_mul_f32 v[36:37], v[34:35], v[44:45] op_sel_hi:[1,0]
	v_mov_b32_e32 v35, 0
	v_pk_mul_f32 v[40:41], v[40:41], v[44:45] op_sel_hi:[1,0]
	v_pk_mul_f32 v[38:39], v[38:39], v[44:45] op_sel_hi:[1,0]
	v_pk_mul_f32 v[48:49], v[56:57], v[44:45] op_sel_hi:[1,0]
	v_pk_mul_f32 v[54:55], v[54:55], v[44:45] op_sel_hi:[1,0]
	v_pk_mul_f32 v[52:53], v[52:53], v[44:45] op_sel_hi:[1,0]
	v_pk_mul_f32 v[44:45], v[50:51], v[44:45] op_sel_hi:[1,0]
	v_mov_b32_e32 v34, 0
	v_cvt_pk_fp8_f32 v35, v36, v37
	v_mov_b32_e32 v36, 0
	v_mov_b32_e32 v37, 0
	v_cvt_pk_fp8_f32 v34, v38, v39
	v_cvt_pk_fp8_f32 v36, v54, v55
	v_cvt_pk_fp8_f32 v37, v44, v45
	v_cvt_pk_fp8_f32 v35, v46, v47 op_sel:[0,0,1]
	v_cvt_pk_fp8_f32 v34, v40, v41 op_sel:[0,0,1]
	v_cvt_pk_fp8_f32 v36, v48, v49 op_sel:[0,0,1]
	v_cvt_pk_fp8_f32 v37, v52, v53 op_sel:[0,0,1]
	v_lshl_add_u32 v38, v42, 10, v144
	global_store_dwordx4 v38, v[34:37], s[4:5]
.LBB0_900:
	s_or_b64 exec, exec, s[14:15]
	s_nop 1
	v_mov_b32_e32 v34, v162
	v_mov_b32_e32 v35, v163
	s_waitcnt lgkmcnt(0)
	v_cmp_lt_i32_e32 vcc, -1, v34
	s_and_saveexec_b64 s[14:15], vcc
	s_cbranch_execz .LBB0_902
	v_mul_f32_e32 v36, 0x3c800000, v35
	v_pk_mul_f32 v[38:39], v[20:21], v[36:37] op_sel_hi:[1,0]
	v_pk_mul_f32 v[20:21], v[18:19], v[36:37] op_sel_hi:[1,0]
	v_mov_b32_e32 v19, 0
	v_pk_mul_f32 v[22:23], v[22:23], v[36:37] op_sel_hi:[1,0]
	v_pk_mul_f32 v[30:31], v[30:31], v[36:37] op_sel_hi:[1,0]
	v_pk_mul_f32 v[26:27], v[26:27], v[36:37] op_sel_hi:[1,0]
	v_mov_b32_e32 v18, 0
	v_cvt_pk_fp8_f32 v19, v20, v21
	v_mov_b32_e32 v20, 0
	v_mov_b32_e32 v21, 0
	v_cvt_pk_fp8_f32 v18, v22, v23
	v_cvt_pk_fp8_f32 v20, v30, v31
	v_cvt_pk_fp8_f32 v21, v26, v27
	v_pk_mul_f32 v[24:25], v[24:25], v[36:37] op_sel_hi:[1,0]
	v_pk_mul_f32 v[32:33], v[32:33], v[36:37] op_sel_hi:[1,0]
	v_pk_mul_f32 v[28:29], v[28:29], v[36:37] op_sel_hi:[1,0]
	v_cvt_pk_fp8_f32 v18, v24, v25 op_sel:[0,0,1]
	v_cvt_pk_fp8_f32 v19, v38, v39 op_sel:[0,0,1]
	v_cvt_pk_fp8_f32 v20, v32, v33 op_sel:[0,0,1]
	v_cvt_pk_fp8_f32 v21, v28, v29 op_sel:[0,0,1]
	v_lshl_add_u32 v22, v34, 10, v144
	global_store_dwordx4 v22, v[18:21], s[4:5]
.LBB0_902:
	s_or_b64 exec, exec, s[14:15]
	s_nop 1
	v_mov_b32_e32 v18, v164
	v_mov_b32_e32 v19, v165
	s_waitcnt lgkmcnt(0)
	v_cmp_lt_i32_e32 vcc, -1, v18
	s_and_saveexec_b64 s[14:15], vcc
	s_cbranch_execz .LBB0_904
	v_mul_f32_e32 v20, 0x3c800000, v19
	v_pk_mul_f32 v[22:23], v[4:5], v[20:21] op_sel_hi:[1,0]
	v_pk_mul_f32 v[4:5], v[2:3], v[20:21] op_sel_hi:[1,0]
	v_mov_b32_e32 v3, 0
	v_pk_mul_f32 v[10:11], v[10:11], v[20:21] op_sel_hi:[1,0]
	v_pk_mul_f32 v[14:15], v[14:15], v[20:21] op_sel_hi:[1,0]
	v_pk_mul_f32 v[6:7], v[6:7], v[20:21] op_sel_hi:[1,0]
	v_mov_b32_e32 v2, 0
	v_cvt_pk_fp8_f32 v3, v4, v5
	v_mov_b32_e32 v4, 0
	v_mov_b32_e32 v5, 0
	v_cvt_pk_fp8_f32 v2, v10, v11
	v_cvt_pk_fp8_f32 v4, v14, v15
	v_cvt_pk_fp8_f32 v5, v6, v7
	v_pk_mul_f32 v[12:13], v[12:13], v[20:21] op_sel_hi:[1,0]
	v_pk_mul_f32 v[16:17], v[16:17], v[20:21] op_sel_hi:[1,0]
	v_pk_mul_f32 v[8:9], v[8:9], v[20:21] op_sel_hi:[1,0]
	v_cvt_pk_fp8_f32 v2, v12, v13 op_sel:[0,0,1]
	v_cvt_pk_fp8_f32 v3, v22, v23 op_sel:[0,0,1]
	v_cvt_pk_fp8_f32 v4, v16, v17 op_sel:[0,0,1]
	v_cvt_pk_fp8_f32 v5, v8, v9 op_sel:[0,0,1]
	v_lshl_add_u32 v6, v18, 10, v144
	global_store_dwordx4 v6, v[2:5], s[4:5]

; #define LAS __attribute__((address_space(3)))
;     __device__ __forceinline__ void operator()(const f32x4 (&acc)[2][2][4][2], const pg8::Unit& u, int wr, int wc, int fr, int fq) const {
;         asm volatile("" : "+v"(fr), "+v"(fq));
;         const unsigned c0b = (unsigned)((u.pn & 3) * 256 + wc * 64 + 16 * fq); const bool shared = (u.pn >> 2) == 256;
;         const LAS u32x2* ri = (const LAS u32x2*)(lds + MOE_RI_OFF) + u.ord * 256 + wr * 64 + fr;
; #pragma unroll
;         for (int ai = 0; ai < 2; ++ai)
; #pragma unroll
;             for (int m = 0; m < 4; ++m) { const u32x2 en = ri[ai * 128 + m * 16]; const float wv = __uint_as_float(en.y) * (YB_SCALE / (H8_SCALE * W8_SCALE));
;                 if ((int)en.x >= 0) { unsigned char* rp = YB + (size_t)(en.x * 1024u + c0b);
;                     const f32x4 v00 = acc[ai][0][m][0] * wv, v01 = acc[ai][0][m][1] * wv, v10 = acc[ai][1][m][0] * wv, v11 = acc[ai][1][m][1] * wv;
;                     const u32x2 h0 = pack8_fp8(v00, v01), h1 = pack8_fp8(v10, v11);
;                     *(u32x4*)rp = (u32x4){h0.x, h0.y, h1.x, h1.y};
.LBB0_2839:
	s_lshl_b32 s15, s55, 11
	v_mov_b32_e32 v144, v138
	v_mov_b32_e32 v130, v137
	s_add_i32 s15, s46, s15
	s_lshl_b32 s14, s14, 8
	v_lshl_add_u32 v145, v130, 3, s15
	ds_read_b64 v[130:131], v145
	ds_read_b64 v[152:153], v145 offset:128
	ds_read_b64 v[154:155], v145 offset:256
	ds_read_b64 v[156:157], v145 offset:384
	ds_read_b64 v[158:159], v145 offset:1024
	ds_read_b64 v[160:161], v145 offset:1152
	ds_read_b64 v[162:163], v145 offset:1280
	ds_read_b64 v[164:165], v145 offset:1408
	s_and_b32 s14, s14, 0x300
	s_or_b32 s14, s14, s45
	v_lshl_add_u32 v144, v144, 4, s14
	s_waitcnt lgkmcnt(0)
	v_cmp_lt_i32_e32 vcc, -1, v130
	s_and_saveexec_b64 s[14:15], vcc
	s_cbranch_execz .LBB0_2841
	v_mul_f32_e32 v146, 0x3c800000, v131
	v_pk_mul_f32 v[148:149], v[116:117], v[146:147] op_sel_hi:[1,0]
	v_pk_mul_f32 v[116:117], v[114:115], v[146:147] op_sel_hi:[1,0]
	v_mov_b32_e32 v114, 0
	v_pk_mul_f32 v[118:119], v[118:119], v[146:147] op_sel_hi:[1,0]
	v_pk_mul_f32 v[122:123], v[122:123], v[146:147] op_sel_hi:[1,0]
	v_pk_mul_f32 v[126:127], v[126:127], v[146:147] op_sel_hi:[1,0]
	v_cvt_pk_fp8_f32 v114, v116, v117
	v_mov_b32_e32 v115, 0
	v_mov_b32_e32 v116, 0
	v_mov_b32_e32 v117, 0
	v_cvt_pk_fp8_f32 v115, v118, v119
	v_cvt_pk_fp8_f32 v116, v122, v123
	v_cvt_pk_fp8_f32 v117, v126, v127
	v_pk_mul_f32 v[120:121], v[120:121], v[146:147] op_sel_hi:[1,0]
	v_pk_mul_f32 v[124:125], v[124:125], v[146:147] op_sel_hi:[1,0]
	v_pk_mul_f32 v[128:129], v[128:129], v[146:147] op_sel_hi:[1,0]
	v_cvt_pk_fp8_f32 v114, v148, v149 op_sel:[0,0,1]
	v_cvt_pk_fp8_f32 v115, v120, v121 op_sel:[0,0,1]
	v_cvt_pk_fp8_f32 v116, v124, v125 op_sel:[0,0,1]
	v_cvt_pk_fp8_f32 v117, v128, v129 op_sel:[0,0,1]
	v_lshl_add_u32 v118, v130, 10, v144
	global_store_dwordx4 v118, v[114:117], s[4:5]
.LBB0_2841:
	s_or_b64 exec, exec, s[14:15]
	s_nop 1
	v_mov_b32_e32 v114, v152
	v_mov_b32_e32 v115, v153
	s_waitcnt lgkmcnt(0)
	v_cmp_lt_i32_e32 vcc, -1, v114
	s_and_saveexec_b64 s[14:15], vcc
	v_readlane_b32 s58, v252, 4
	v_readlane_b32 s59, v252, 5
	s_cbranch_execz .LBB0_2843
	v_mul_f32_e32 v116, 0x3c800000, v115
	v_pk_mul_f32 v[118:119], v[100:101], v[116:117] op_sel_hi:[1,0]
	v_pk_mul_f32 v[100:101], v[98:99], v[116:117] op_sel_hi:[1,0]
	v_mov_b32_e32 v99, 0
	v_pk_mul_f32 v[102:103], v[102:103], v[116:117] op_sel_hi:[1,0]
	v_pk_mul_f32 v[110:111], v[110:111], v[116:117] op_sel_hi:[1,0]
	v_pk_mul_f32 v[106:107], v[106:107], v[116:117] op_sel_hi:[1,0]
	v_mov_b32_e32 v98, 0
	v_cvt_pk_fp8_f32 v99, v100, v101
	v_mov_b32_e32 v100, 0
	v_mov_b32_e32 v101, 0
	v_cvt_pk_fp8_f32 v98, v102, v103
	v_cvt_pk_fp8_f32 v100, v110, v111
	v_cvt_pk_fp8_f32 v101, v106, v107
	v_pk_mul_f32 v[104:105], v[104:105], v[116:117] op_sel_hi:[1,0]
	v_pk_mul_f32 v[112:113], v[112:113], v[116:117] op_sel_hi:[1,0]
	v_pk_mul_f32 v[108:109], v[108:109], v[116:117] op_sel_hi:[1,0]
	v_cvt_pk_fp8_f32 v98, v104, v105 op_sel:[0,0,1]
	v_cvt_pk_fp8_f32 v99, v118, v119 op_sel:[0,0,1]
	v_cvt_pk_fp8_f32 v100, v112, v113 op_sel:[0,0,1]
	v_cvt_pk_fp8_f32 v101, v108, v109 op_sel:[0,0,1]
	v_lshl_add_u32 v102, v114, 10, v144
	global_store_dwordx4 v102, v[98:101], s[4:5]
